# static priority raise for waves 4-7 in gqa16 plus counted waits in both attention pass prologues (K(1) loads issued with the Q/K(0)/V(0) loads)
# baseline (speedup 1.0000x reference)
; #define HLOADV(kt) do { const char* vb_ = (const char*)Vh + (size_t)(kt) * (64 * LDK * 2); sv0 = *(const bf16x8*)(vb_ + koff0); sv1 = *(const bf16x8*)(vb_ + koff1); } while (0)
; #define HLOADK(kt) do { const char* kb_ = (const char*)Kh + (size_t)(kt) * (64 * LDK * 2); sk0 = *(const bf16x8*)(kb_ + koff0); sk1 = *(const bf16x8*)(kb_ + koff1); } while (0)
; #define HWRITEV(b) do { char* d_ = V_lds + (b) * G16_V; *(bf16x8*)(d_ + vst0) = sv0; *(bf16x8*)(d_ + vst1) = sv1; } while (0)
; #define HWRITEK(b) do { char* d_ = K_lds + (b) * GB_K; *(bf16x8*)(d_ + KSWZ(sr, sc * 2)) = sk0; *(bf16x8*)(d_ + KSWZ(32 + sr, sc * 2)) = sk1; } while (0)
; #define HEXP() do { _Pragma("unroll") for (int kt = 0; kt < 4; ++kt) { _Pragma("unroll") for (int qt = 0; qt < 2; ++qt) { _Pragma("unroll") for (int i = 0; i < 4; ++i) s[kt][qt][i] = __builtin_amdgcn_exp2f(fmaf(s[kt][qt][i], C, mnC)); } } } while (0)
; template <int LDQ, int LDK, int LDO>
; __device__ __forceinline__ void attn_gqa16_body(const bf16* __restrict__ Qb, const bf16* __restrict__ Kh, const bf16* __restrict__ Vh, bf16* __restrict__ Ob, int seq, char* lds, float mref) {
;     ...
;   { int l16q = l16, gq = g, widq = wid; asm volatile("" : "+v"(l16q), "+v"(gq), "+v"(widq));
;     const bf16* Qw = Qb + (widq >> 2) * 128 + (long)((widq & 3) * QBLK + l16q) * LDQ + gq * 8;
; #pragma unroll
;     for (int qt = 0; qt < 2; ++qt)
; #pragma unroll
;       for (int ds = 0; ds < 4; ++ds) qr[qt][ds] = *reinterpret_cast<const bf16x8*>(Qw + (long)qt * 16 * LDQ + ds * 32); }
;   const int sr = tid >> 4, sc = (tid & 15) * 8;
;   const int vst0 = (sc >> 4) * VP16 + sr * 32 + ((sc >> 3) & 1) * 16, vst1 = vst0 + 1024;
;   const int vb0 = (int)(uintptr_t)V_lds + (4 * g + (l16 >> 2)) * 32 + (l16 & 3) * 8;
;   const int kb0 = l16 * 272 + g * 16;
;   bf16x8 sv0, sv1, sk0, sk1;
;   const unsigned koff0 = (unsigned)(sr * LDK + sc) * 2u, koff1 = koff0 + 32u * LDK * 2u;
;     ...
;   f32x4a s[4][2]; bf16x8 pb[2][2];
;     ...
;   const int NT = seq / KVBLK;
;   HLOADK(0); HLOADV(0); asm volatile("s_waitcnt vmcnt(0)" ::: "memory"); HWRITEK(0); HWRITEV(0);
;   HLOADK(1); asm volatile("s_waitcnt vmcnt(0)" ::: "memory"); HWRITEK(1); __syncthreads();
;   HLOADK(2); HLOADV(1);
;   HQK(0); HEXP();
.LBB0_646:
	s_and_b64 vcc, exec, s[14:15]
	s_cbranch_vccz .LBB0_641
	s_lshl_b32 s8, s45, 7
	s_and_b32 s8, s8, 0x3f80
	s_ashr_i32 s14, s45, 8
	s_mul_i32 s12, s8, 0x2400
	s_add_u32 s15, s33, s12
	s_addc_u32 s17, s35, 0
	s_lshl_b32 s13, s45, 1
	s_lshl_b32 s12, s14, 9
	s_and_b32 s13, s13, 0x100
	s_or_b32 s12, s12, s13
	s_ashr_i32 s13, s12, 31
	v_mov_b32_e32 v4, v180
	v_mov_b32_e32 v2, v185
	v_mov_b32_e32 v5, v176
	s_lshl_b64 s[12:13], s[12:13], 1
	s_add_u32 s16, s15, s12
	v_lshlrev_b32_e32 v6, 5, v2
	v_and_b32_e32 v2, 0xffffff80, v6
	s_addc_u32 s17, s17, s13
	v_ashrrev_i32_e32 v3, 31, v2
	v_and_b32_e32 v6, 0x60, v6
	s_lshl_b32 s14, s14, 7
	v_lshl_add_u64 v[2:3], v[2:3], 1, s[16:17]
	v_add_u32_e32 v4, v6, v4
	s_ashr_i32 s15, s14, 31
	v_mad_i64_i32 v[2:3], s[16:17], v4, s26, v[2:3]
	v_lshlrev_b32_e32 v4, 3, v5
	s_lshl_b64 s[46:47], s[14:15], 1
	v_ashrrev_i32_e32 v5, 31, v4
	s_add_u32 s48, s21, s46
	v_lshl_add_u64 v[6:7], v[4:5], 1, v[2:3]
	s_addc_u32 s49, s22, s47
	global_load_dwordx4 v[30:33], v[6:7], off
	global_load_dwordx4 v[18:21], v[6:7], off offset:64
	global_load_dwordx4 v[10:13], v[6:7], off offset:128
	global_load_dwordx4 v[2:5], v[6:7], off offset:192
	v_add_co_u32_e32 v6, vcc, s27, v6
	s_add_u32 s46, s23, s46
	s_nop 0
	v_addc_co_u32_e32 v7, vcc, 0, v7, vcc
	v_lshl_add_u64 v[102:103], s[48:49], 0, v[178:179]
	s_addc_u32 s47, s24, s47
	s_add_u32 s74, s46, 0x90000
	s_addc_u32 s75, s47, 0
	s_add_u32 s76, s74, 0x48000
	s_addc_u32 s77, s75, 0
	v_add_co_u32_e32 v34, vcc, s28, v102
	v_lshl_add_u64 v[104:105], s[46:47], 0, v[178:179]
	s_nop 0
	v_addc_co_u32_e32 v35, vcc, 0, v103, vcc
	v_add_co_u32_e32 v46, vcc, s28, v104
	global_load_dwordx4 v[38:41], v[6:7], off
	global_load_dwordx4 v[22:25], v[6:7], off offset:64
	global_load_dwordx4 v[14:17], v[6:7], off offset:128
	s_nop 0
	global_load_dwordx4 v[6:9], v[6:7], off offset:192
	v_addc_co_u32_e32 v47, vcc, 0, v105, vcc
	v_add_co_u32_e32 v50, vcc, s29, v102
	global_load_dwordx4 v[26:29], v[102:103], off
	s_nop 0
	global_load_dwordx4 v[34:37], v[34:35], off
	v_addc_co_u32_e32 v51, vcc, 0, v103, vcc
	v_add_co_u32_e32 v54, vcc, s30, v102
	global_load_dwordx4 v[42:45], v[104:105], off
	s_nop 0
	global_load_dwordx4 v[46:49], v[46:47], off
	v_addc_co_u32_e32 v55, vcc, 0, v103, vcc
	global_load_dwordx4 v[50:53], v[50:51], off
	s_nop 0
	global_load_dwordx4 v[54:57], v[54:55], off
	s_waitcnt vmcnt(5)
	ds_write_b128 v194, v[26:29] offset:33280
	s_waitcnt vmcnt(4)
	ds_write_b128 v194, v[34:37] offset:41984
	s_waitcnt vmcnt(3)
	ds_write_b128 v181, v[42:45]
	s_waitcnt vmcnt(2)
	ds_write_b128 v181, v[46:49] offset:1024
	s_waitcnt vmcnt(0)
	s_waitcnt vmcnt(1)
	ds_write_b128 v194, v[50:53] offset:50688
	s_waitcnt vmcnt(0)
	ds_write_b128 v194, v[54:57] offset:59392
	s_waitcnt lgkmcnt(0)
	s_barrier
	ds_read_b128 v[26:29], v182 offset:33280
	ds_read_b128 v[34:37], v182 offset:33344
	ds_read_b128 v[46:49], v182 offset:37632
	ds_read_b128 v[50:53], v182 offset:37696
	ds_read_b128 v[58:61], v182 offset:41984
	ds_read_b128 v[62:65], v182 offset:42048
	ds_read_b128 v[70:73], v182 offset:46336
	ds_read_b128 v[74:77], v182 offset:46400
	s_waitcnt lgkmcnt(7)
	v_mfma_f32_16x16x32_bf16 v[42:45], v[26:29], v[30:33], 0
	v_mfma_f32_16x16x32_bf16 v[26:29], v[26:29], v[38:41], 0
	s_waitcnt lgkmcnt(5)
	v_mfma_f32_16x16x32_bf16 v[54:57], v[46:49], v[30:33], 0
	v_mfma_f32_16x16x32_bf16 v[46:49], v[46:49], v[38:41], 0
	s_waitcnt lgkmcnt(3)
	v_mfma_f32_16x16x32_bf16 v[66:69], v[58:61], v[30:33], 0
	v_mfma_f32_16x16x32_bf16 v[58:61], v[58:61], v[38:41], 0
	s_waitcnt lgkmcnt(1)
	v_mfma_f32_16x16x32_bf16 v[78:81], v[70:73], v[30:33], 0
	v_mfma_f32_16x16x32_bf16 v[70:73], v[70:73], v[38:41], 0
	v_mfma_f32_16x16x32_bf16 v[42:45], v[34:37], v[18:21], v[42:45]
	v_mfma_f32_16x16x32_bf16 v[26:29], v[34:37], v[22:25], v[26:29]
	v_mfma_f32_16x16x32_bf16 v[34:37], v[50:53], v[18:21], v[54:57]
	v_mfma_f32_16x16x32_bf16 v[46:49], v[50:53], v[22:25], v[46:49]
	v_mfma_f32_16x16x32_bf16 v[50:53], v[62:65], v[18:21], v[66:69]
	v_mfma_f32_16x16x32_bf16 v[54:57], v[62:65], v[22:25], v[58:61]
	s_waitcnt lgkmcnt(0)
	v_mfma_f32_16x16x32_bf16 v[58:61], v[74:77], v[18:21], v[78:81]
	v_mfma_f32_16x16x32_bf16 v[62:65], v[74:77], v[22:25], v[70:73]
	ds_read_b128 v[66:69], v182 offset:33408
	ds_read_b128 v[74:77], v182 offset:33472
	s_waitcnt lgkmcnt(1)
	v_mfma_f32_16x16x32_bf16 v[42:45], v[66:69], v[10:13], v[42:45]
	v_mfma_f32_16x16x32_bf16 v[26:29], v[66:69], v[14:17], v[26:29]
	ds_read_b128 v[66:69], v182 offset:37760
	ds_read_b128 v[78:81], v182 offset:37824
	s_waitcnt lgkmcnt(1)
	v_mfma_f32_16x16x32_bf16 v[34:37], v[66:69], v[10:13], v[34:37]
	v_mfma_f32_16x16x32_bf16 v[46:49], v[66:69], v[14:17], v[46:49]
	ds_read_b128 v[66:69], v182 offset:42112
	ds_read_b128 v[82:85], v182 offset:42176
	s_waitcnt lgkmcnt(1)
	v_mfma_f32_16x16x32_bf16 v[50:53], v[66:69], v[10:13], v[50:53]
	v_mfma_f32_16x16x32_bf16 v[86:89], v[66:69], v[14:17], v[54:57]
	s_nop 2
	ds_read_b128 v[54:57], v182 offset:46464
	ds_read_b128 v[90:93], v182 offset:46528
	v_mfma_f32_16x16x32_bf16 v[66:69], v[74:77], v[6:9], v[26:29]
	s_nop 2
	v_add_co_u32_e32 v26, vcc, s25, v102
	s_waitcnt lgkmcnt(1)
; #define HLOADV(kt) do { const char* vb_ = (const char*)Vh + (size_t)(kt) * (64 * LDK * 2); sv0 = *(const bf16x8*)(vb_ + koff0); sv1 = *(const bf16x8*)(vb_ + koff1); } while (0)
; #define HLOADK(kt) do { const char* kb_ = (const char*)Kh + (size_t)(kt) * (64 * LDK * 2); sk0 = *(const bf16x8*)(kb_ + koff0); sk1 = *(const bf16x8*)(kb_ + koff1); } while (0)
; #define HWRITEV(b) do { char* d_ = V_lds + (b) * G16_V; *(bf16x8*)(d_ + vst0) = sv0; *(bf16x8*)(d_ + vst1) = sv1; } while (0)
; #define HWRITEK(b) do { char* d_ = K_lds + (b) * GB_K; *(bf16x8*)(d_ + KSWZ(sr, sc * 2)) = sk0; *(bf16x8*)(d_ + KSWZ(32 + sr, sc * 2)) = sk1; } while (0)
; #define HEXP() do { _Pragma("unroll") for (int kt = 0; kt < 4; ++kt) { _Pragma("unroll") for (int qt = 0; qt < 2; ++qt) { _Pragma("unroll") for (int i = 0; i < 4; ++i) s[kt][qt][i] = __builtin_amdgcn_exp2f(fmaf(s[kt][qt][i], C, mnC)); } } } while (0)
; template <int LDQ, int LDK, int LDO>
; __device__ __forceinline__ void attn_gqa16_body(const bf16* __restrict__ Qb, const bf16* __restrict__ Kh, const bf16* __restrict__ Vh, bf16* __restrict__ Ob, int seq, char* lds, float mref) {
;     ...
;   const int NT = seq / KVBLK;
;   HLOADK(0); HLOADV(0); asm volatile("s_waitcnt vmcnt(0)" ::: "memory"); HWRITEK(0); HWRITEV(0);
;   HLOADK(1); asm volatile("s_waitcnt vmcnt(0)" ::: "memory"); HWRITEK(1); __syncthreads();
;   HLOADK(2); HLOADV(1);
;   HQK(0); HEXP();
;   if (wid >= 4) __builtin_amdgcn_s_setprio(1);
;   for (int t = 0; t < NT; ++t) {
;     HPACK();
;     __syncthreads();
	v_mfma_f32_16x16x32_bf16 v[98:101], v[54:57], v[14:17], v[62:65]
	v_addc_co_u32_e32 v27, vcc, 0, v103, vcc
	v_add_co_u32_e32 v28, vcc, s31, v102
	v_mfma_f32_16x16x32_bf16 v[62:65], v[78:81], v[2:5], v[34:37]
	s_nop 0
	v_addc_co_u32_e32 v29, vcc, 0, v103, vcc
	global_load_dwordx4 v[106:109], v[26:27], off
	global_load_dwordx4 v[110:113], v[28:29], off
	v_add_co_u32_e32 v26, vcc, s29, v104
	v_mfma_f32_16x16x32_bf16 v[94:97], v[54:57], v[10:13], v[58:61]
	s_nop 0
	v_addc_co_u32_e32 v27, vcc, 0, v105, vcc
	v_add_co_u32_e32 v34, vcc, s30, v104
	v_mfma_f32_16x16x32_bf16 v[70:73], v[74:77], v[2:5], v[42:45]
	s_nop 0
	v_addc_co_u32_e32 v35, vcc, 0, v105, vcc
	s_nop 0
	v_mfma_f32_16x16x32_bf16 v[58:61], v[78:81], v[6:9], v[46:49]
	v_mfma_f32_16x16x32_bf16 v[54:57], v[82:85], v[2:5], v[50:53]
	v_mfma_f32_16x16x32_bf16 v[50:53], v[82:85], v[6:9], v[86:89]
	s_waitcnt lgkmcnt(0)
	v_mfma_f32_16x16x32_bf16 v[46:49], v[90:93], v[2:5], v[94:97]
	v_mfma_f32_16x16x32_bf16 v[42:45], v[90:93], v[6:9], v[98:101]
	s_and_saveexec_b64 s[16:17], s[4:5]
	s_setprio 1
	s_or_b64 exec, exec, s[16:17]
	v_add_f32_e32 v70, v186, v70
	v_add_f32_e32 v66, v186, v66
	v_add_f32_e32 v62, v186, v62
	v_add_f32_e32 v58, v186, v58
	v_add_f32_e32 v54, v186, v54
	v_add_f32_e32 v50, v186, v50
	v_add_f32_e32 v46, v186, v46
	v_add_f32_e32 v42, v186, v42
	v_exp_f32_e32 v158, v70
	v_add_f32_e32 v70, v186, v71
	v_exp_f32_e32 v159, v66
	v_add_f32_e32 v66, v186, v67
	v_exp_f32_e32 v168, v62
	v_add_f32_e32 v62, v186, v63
	v_exp_f32_e32 v169, v58
	v_add_f32_e32 v58, v186, v59
	v_exp_f32_e32 v142, v54
	v_add_f32_e32 v54, v186, v55
	v_exp_f32_e32 v143, v50
	v_add_f32_e32 v50, v186, v51
	v_exp_f32_e32 v134, v46
	v_add_f32_e32 v46, v186, v47
	v_exp_f32_e32 v135, v42
	v_add_f32_e32 v42, v186, v43
	v_exp_f32_e32 v152, v70
	v_add_f32_e32 v70, v186, v72
	v_exp_f32_e32 v153, v66
	v_add_f32_e32 v66, v186, v68
	v_exp_f32_e32 v170, v62
	v_add_f32_e32 v62, v186, v64
	v_exp_f32_e32 v171, v58
	v_add_f32_e32 v58, v186, v60
	v_exp_f32_e32 v172, v54
	v_add_f32_e32 v54, v186, v56
	v_exp_f32_e32 v173, v50
	v_add_f32_e32 v50, v186, v52
	v_exp_f32_e32 v138, v46
	v_add_f32_e32 v46, v186, v48
	v_exp_f32_e32 v139, v42
	v_add_f32_e32 v42, v186, v44
	v_exp_f32_e32 v156, v70
	v_add_f32_e32 v70, v186, v73
	v_exp_f32_e32 v157, v66
	v_add_f32_e32 v66, v186, v69
	v_exp_f32_e32 v164, v62
	v_add_f32_e32 v62, v186, v65
	v_exp_f32_e32 v165, v58
	v_add_f32_e32 v58, v186, v61
	v_exp_f32_e32 v144, v54
	v_add_f32_e32 v54, v186, v57
	v_exp_f32_e32 v145, v50
	v_add_f32_e32 v50, v186, v53
	v_exp_f32_e32 v136, v46
	v_add_f32_e32 v46, v186, v49
	v_exp_f32_e32 v137, v42
	v_add_f32_e32 v42, v186, v45
	v_exp_f32_e32 v160, v70
	v_exp_f32_e32 v161, v66
	v_exp_f32_e32 v166, v62
	v_exp_f32_e32 v167, v58
	v_exp_f32_e32 v174, v54
	v_exp_f32_e32 v175, v50
	v_exp_f32_e32 v140, v46
	v_exp_f32_e32 v141, v42
	v_mov_b32_e32 v50, 0
	v_lshl_add_u64 v[162:163], s[14:15], 1, v[154:155]
	s_mov_b32 s16, 0
	s_mov_b64 s[14:15], 0
	v_mov_b32_e32 v51, v50
	v_mov_b32_e32 v52, v50
	v_mov_b32_e32 v53, v50
	v_mov_b32_e32 v78, v50
	v_mov_b32_e32 v79, v50
	v_mov_b32_e32 v80, v50
	v_mov_b32_e32 v81, v50
	v_mov_b32_e32 v90, v50
	v_mov_b32_e32 v91, v50
	v_mov_b32_e32 v92, v50
	v_mov_b32_e32 v93, v50
	v_mov_b32_e32 v94, v50
	v_mov_b32_e32 v95, v50
	v_mov_b32_e32 v96, v50
	v_mov_b32_e32 v97, v50
	v_mov_b32_e32 v98, v50
	v_mov_b32_e32 v99, v50
	v_mov_b32_e32 v100, v50
	v_mov_b32_e32 v101, v50
	v_mov_b32_e32 v102, v50
	v_mov_b32_e32 v103, v50
	v_mov_b32_e32 v104, v50
	v_mov_b32_e32 v105, v50
	v_mov_b32_e32 v82, v50
	v_mov_b32_e32 v83, v50
	v_mov_b32_e32 v84, v50
	v_mov_b32_e32 v85, v50
	v_mov_b32_e32 v86, v50
	v_mov_b32_e32 v87, v50
	v_mov_b32_e32 v88, v50
	v_mov_b32_e32 v89, v50
	v_mov_b32_e32 v54, v50
	v_mov_b32_e32 v55, v50
	v_mov_b32_e32 v56, v50
	v_mov_b32_e32 v57, v50
	v_mov_b32_e32 v62, v50
	v_mov_b32_e32 v63, v50
	v_mov_b32_e32 v64, v50
	v_mov_b32_e32 v65, v50
	v_mov_b32_e32 v58, v50
	v_mov_b32_e32 v59, v50
	v_mov_b32_e32 v60, v50
	v_mov_b32_e32 v61, v50
	v_mov_b32_e32 v70, v50
	v_mov_b32_e32 v71, v50
	v_mov_b32_e32 v72, v50
	v_mov_b32_e32 v73, v50
	v_mov_b32_e32 v42, v50
	v_mov_b32_e32 v43, v50
	v_mov_b32_e32 v44, v50
	v_mov_b32_e32 v45, v50
	v_mov_b32_e32 v46, v50
	v_mov_b32_e32 v47, v50
	v_mov_b32_e32 v48, v50
	v_mov_b32_e32 v49, v50
	v_mov_b32_e32 v66, v50
	v_mov_b32_e32 v67, v50
	v_mov_b32_e32 v68, v50
	v_mov_b32_e32 v69, v50
	v_mov_b32_e32 v74, v50
	v_mov_b32_e32 v75, v50
	v_mov_b32_e32 v76, v50
	v_mov_b32_e32 v77, v50
	v_mov_b32_e32 v150, v50
	v_mov_b32_e32 v151, v50
	s_cmp_ge_u32 s84, 0x2080
	s_cbranch_scc0 .Lvg_prio
	s_setprio 2
.Lvg_prio:
	v_mov_b32_e32 v240, v156
	v_mov_b32_e32 v241, v157
	v_mov_b32_e32 v246, v158
	v_mov_b32_e32 v247, v159
	v_mov_b32_e32 v242, v164
	v_mov_b32_e32 v243, v165
	v_mov_b32_e32 v244, v166
	v_mov_b32_e32 v245, v167
	s_nop 0
	s_nop 0
	s_nop 0
	s_nop 0
